# MoBA attention S = K Q^T: K fragment reads run seven MFMAs ahead through eight quads (idle P.V registers) with counted lgkmcnt waits; all four tile-loop variants
# speedup vs baseline: 1.0029x; 1.0029x over previous
.LBB0_711:
	v_add_u32_e32 v208, v177, v162
	ds_read_b128 v[200:203], v208 offset:4096
	ds_read_b128 v[204:207], v208 offset:12800
	ds_read_b128 v[210:213], v208 offset:4128
	ds_read_b128 v[214:217], v208 offset:12832
	ds_read_b128 v[218:221], v208 offset:4160
	ds_read_b128 v[222:225], v208 offset:12864
	ds_read_b128 v[226:229], v208 offset:4192
	ds_read_b128 v[230:233], v208 offset:12896
	s_andn2_b64 vcc, exec, s[4:5]
	s_waitcnt lgkmcnt(7)
	v_mfma_f32_32x32x16_bf16 v[82:97], v[200:203], v[102:105], 0
	ds_read_b128 v[200:203], v208 offset:4224
	s_waitcnt lgkmcnt(7)
	v_mfma_f32_32x32x16_bf16 v[66:81], v[204:207], v[102:105], 0
	ds_read_b128 v[204:207], v208 offset:12928
	s_waitcnt lgkmcnt(7)
	v_mfma_f32_32x32x16_bf16 v[82:97], v[210:213], v[98:101], v[82:97]
	ds_read_b128 v[210:213], v208 offset:4256
	s_waitcnt lgkmcnt(7)
	v_mfma_f32_32x32x16_bf16 v[66:81], v[214:217], v[98:101], v[66:81]
	ds_read_b128 v[214:217], v208 offset:12960
	s_waitcnt lgkmcnt(7)
	v_mfma_f32_32x32x16_bf16 v[82:97], v[218:221], v[110:113], v[82:97]
	ds_read_b128 v[218:221], v208 offset:4288
	s_waitcnt lgkmcnt(7)
	v_mfma_f32_32x32x16_bf16 v[66:81], v[222:225], v[110:113], v[66:81]
	ds_read_b128 v[222:225], v208 offset:12992
	s_waitcnt lgkmcnt(7)
	v_mfma_f32_32x32x16_bf16 v[82:97], v[226:229], v[106:109], v[82:97]
	ds_read_b128 v[226:229], v208 offset:4320
	s_waitcnt lgkmcnt(7)
	v_mfma_f32_32x32x16_bf16 v[66:81], v[230:233], v[106:109], v[66:81]
	ds_read_b128 v[230:233], v208 offset:13024
	s_waitcnt lgkmcnt(7)
	v_mfma_f32_32x32x16_bf16 v[82:97], v[200:203], v[118:121], v[82:97]
	s_waitcnt lgkmcnt(6)
	v_mfma_f32_32x32x16_bf16 v[66:81], v[204:207], v[118:121], v[66:81]
	s_waitcnt lgkmcnt(5)
	v_mfma_f32_32x32x16_bf16 v[82:97], v[210:213], v[114:117], v[82:97]
	s_waitcnt lgkmcnt(4)
	v_mfma_f32_32x32x16_bf16 v[66:81], v[214:217], v[114:117], v[66:81]
	s_waitcnt lgkmcnt(3)
	v_mfma_f32_32x32x16_bf16 v[82:97], v[218:221], v[126:129], v[82:97]
	s_waitcnt lgkmcnt(2)
	v_mfma_f32_32x32x16_bf16 v[66:81], v[222:225], v[126:129], v[66:81]
	v_cndmask_b32_e64 v196, 0, 1, s[4:5]
	v_cmp_ne_u32_e64 s[6:7], 1, v196
	s_waitcnt lgkmcnt(1)
	v_mfma_f32_32x32x16_bf16 v[82:97], v[226:229], v[122:125], v[82:97]
	s_waitcnt lgkmcnt(0)
	v_mfma_f32_32x32x16_bf16 v[66:81], v[230:233], v[122:125], v[66:81]
	s_cbranch_vccnz .LBB0_713
	v_cmp_lt_i32_e32 vcc, v175, v194
	s_nop 7
	v_cndmask_b32_e32 v83, v169, v83, vcc
	v_cmp_le_i32_e32 vcc, v175, v194
	s_nop 1
	v_cndmask_b32_e32 v82, v169, v82, vcc
	v_cmp_le_i32_e32 vcc, v180, v194
	s_nop 1
	v_cndmask_b32_e32 v84, v169, v84, vcc
	v_cmp_le_i32_e32 vcc, v181, v194
	s_nop 1
	v_cndmask_b32_e32 v85, v169, v85, vcc
	v_cmp_le_i32_e32 vcc, v182, v194
	s_nop 1
	v_cndmask_b32_e32 v86, v169, v86, vcc
	v_cmp_le_i32_e32 vcc, v183, v194
	s_nop 1
	v_cndmask_b32_e32 v87, v169, v87, vcc
	v_cmp_le_i32_e32 vcc, v184, v194
	s_nop 1
	v_cndmask_b32_e32 v88, v169, v88, vcc
	v_cmp_le_i32_e32 vcc, v185, v194
	s_nop 1
	v_cndmask_b32_e32 v89, v169, v89, vcc
	v_cmp_le_i32_e32 vcc, v186, v194
	s_nop 1
	v_cndmask_b32_e32 v90, v169, v90, vcc
	v_cmp_le_i32_e32 vcc, v187, v194
	s_nop 1
	v_cndmask_b32_e32 v91, v169, v91, vcc
	v_cmp_le_i32_e32 vcc, v188, v194
	s_nop 1
	v_cndmask_b32_e32 v92, v169, v92, vcc
	v_cmp_le_i32_e32 vcc, v189, v194
	s_nop 1
	v_cndmask_b32_e32 v93, v169, v93, vcc
	v_cmp_le_i32_e32 vcc, v190, v194
	s_nop 1
	v_cndmask_b32_e32 v94, v169, v94, vcc
	v_cmp_le_i32_e32 vcc, v191, v194
	s_nop 1
	v_cndmask_b32_e32 v95, v169, v95, vcc
	v_cmp_le_i32_e32 vcc, v192, v194
	s_nop 1
	v_cndmask_b32_e32 v96, v169, v96, vcc
	v_cmp_le_i32_e32 vcc, v193, v194
	s_nop 1
	v_cndmask_b32_e32 v97, v169, v97, vcc

.LBB0_738:
	v_add_u32_e32 v208, v177, v162
	ds_read_b128 v[200:203], v208 offset:21504
	ds_read_b128 v[204:207], v208 offset:30208
	ds_read_b128 v[210:213], v208 offset:21536
	ds_read_b128 v[214:217], v208 offset:30240
	ds_read_b128 v[218:221], v208 offset:21568
	ds_read_b128 v[222:225], v208 offset:30272
	ds_read_b128 v[226:229], v208 offset:21600
	ds_read_b128 v[230:233], v208 offset:30304
	s_andn2_b64 vcc, exec, s[6:7]
	s_waitcnt lgkmcnt(7)
	v_mfma_f32_32x32x16_bf16 v[82:97], v[200:203], v[102:105], 0
	ds_read_b128 v[200:203], v208 offset:21632
	s_waitcnt lgkmcnt(7)
	v_mfma_f32_32x32x16_bf16 v[66:81], v[204:207], v[102:105], 0
	ds_read_b128 v[204:207], v208 offset:30336
	s_waitcnt lgkmcnt(7)
	v_mfma_f32_32x32x16_bf16 v[82:97], v[210:213], v[98:101], v[82:97]
	ds_read_b128 v[210:213], v208 offset:21664
	s_waitcnt lgkmcnt(7)
	v_mfma_f32_32x32x16_bf16 v[66:81], v[214:217], v[98:101], v[66:81]
	ds_read_b128 v[214:217], v208 offset:30368
	s_waitcnt lgkmcnt(7)
	v_mfma_f32_32x32x16_bf16 v[82:97], v[218:221], v[110:113], v[82:97]
	ds_read_b128 v[218:221], v208 offset:21696
	s_waitcnt lgkmcnt(7)
	v_mfma_f32_32x32x16_bf16 v[66:81], v[222:225], v[110:113], v[66:81]
	ds_read_b128 v[222:225], v208 offset:30400
	s_waitcnt lgkmcnt(7)
	v_mfma_f32_32x32x16_bf16 v[82:97], v[226:229], v[106:109], v[82:97]
	ds_read_b128 v[226:229], v208 offset:21728
	s_waitcnt lgkmcnt(7)
	v_mfma_f32_32x32x16_bf16 v[66:81], v[230:233], v[106:109], v[66:81]
	ds_read_b128 v[230:233], v208 offset:30432
	s_waitcnt lgkmcnt(7)
	v_mfma_f32_32x32x16_bf16 v[82:97], v[200:203], v[118:121], v[82:97]
	s_waitcnt lgkmcnt(6)
	v_mfma_f32_32x32x16_bf16 v[66:81], v[204:207], v[118:121], v[66:81]
	s_waitcnt lgkmcnt(5)
	v_mfma_f32_32x32x16_bf16 v[82:97], v[210:213], v[114:117], v[82:97]
	s_waitcnt lgkmcnt(4)
	v_mfma_f32_32x32x16_bf16 v[66:81], v[214:217], v[114:117], v[66:81]
	s_waitcnt lgkmcnt(3)
	v_mfma_f32_32x32x16_bf16 v[82:97], v[218:221], v[126:129], v[82:97]
	s_waitcnt lgkmcnt(2)
	v_mfma_f32_32x32x16_bf16 v[66:81], v[222:225], v[126:129], v[66:81]
	v_cndmask_b32_e64 v196, 0, 1, s[6:7]
	v_cmp_ne_u32_e64 s[4:5], 1, v196
	s_waitcnt lgkmcnt(1)
	v_mfma_f32_32x32x16_bf16 v[82:97], v[226:229], v[122:125], v[82:97]
	s_waitcnt lgkmcnt(0)
	v_mfma_f32_32x32x16_bf16 v[66:81], v[230:233], v[122:125], v[66:81]
	s_cbranch_vccnz .LBB0_740
	v_subrev_u32_e32 v196, 64, v194
	v_cmp_lt_i32_e32 vcc, v175, v196
	s_nop 6
	v_cndmask_b32_e32 v83, v169, v83, vcc
	v_cmp_le_i32_e32 vcc, v175, v196
	s_nop 1
	v_cndmask_b32_e32 v82, v169, v82, vcc
	v_cmp_le_i32_e32 vcc, v180, v196
	s_nop 1
	v_cndmask_b32_e32 v84, v169, v84, vcc
	v_cmp_le_i32_e32 vcc, v181, v196
	s_nop 1
	v_cndmask_b32_e32 v85, v169, v85, vcc
	v_cmp_le_i32_e32 vcc, v182, v196
	s_nop 1
	v_cndmask_b32_e32 v86, v169, v86, vcc
	v_cmp_le_i32_e32 vcc, v183, v196
	s_nop 1
	v_cndmask_b32_e32 v87, v169, v87, vcc
	v_cmp_le_i32_e32 vcc, v184, v196
	s_nop 1
	v_cndmask_b32_e32 v88, v169, v88, vcc
	v_cmp_le_i32_e32 vcc, v185, v196
	s_nop 1
	v_cndmask_b32_e32 v89, v169, v89, vcc
	v_cmp_le_i32_e32 vcc, v186, v196
	s_nop 1
	v_cndmask_b32_e32 v90, v169, v90, vcc
	v_cmp_le_i32_e32 vcc, v187, v196
	s_nop 1
	v_cndmask_b32_e32 v91, v169, v91, vcc
	v_cmp_le_i32_e32 vcc, v188, v196
	s_nop 1
	v_cndmask_b32_e32 v92, v169, v92, vcc
	v_cmp_le_i32_e32 vcc, v189, v196
	s_nop 1
	v_cndmask_b32_e32 v93, v169, v93, vcc
	v_cmp_le_i32_e32 vcc, v190, v196
	s_nop 1
	v_cndmask_b32_e32 v94, v169, v94, vcc
	v_cmp_le_i32_e32 vcc, v191, v196
	s_nop 1
	v_cndmask_b32_e32 v95, v169, v95, vcc
	v_cmp_le_i32_e32 vcc, v192, v196
	s_nop 1
	v_cndmask_b32_e32 v96, v169, v96, vcc
	v_cmp_le_i32_e32 vcc, v193, v196
	s_nop 1
	v_cndmask_b32_e32 v97, v169, v97, vcc

.LBB0_1783:
	v_add_u32_e32 v208, v177, v162
	ds_read_b128 v[200:203], v208 offset:4096
	ds_read_b128 v[204:207], v208 offset:12800
	ds_read_b128 v[210:213], v208 offset:4128
	ds_read_b128 v[214:217], v208 offset:12832
	ds_read_b128 v[218:221], v208 offset:4160
	ds_read_b128 v[222:225], v208 offset:12864
	ds_read_b128 v[226:229], v208 offset:4192
	ds_read_b128 v[230:233], v208 offset:12896
	s_andn2_b64 vcc, exec, s[6:7]
	s_waitcnt lgkmcnt(7)
	v_mfma_f32_32x32x16_bf16 v[82:97], v[200:203], v[102:105], 0
	ds_read_b128 v[200:203], v208 offset:4224
	s_waitcnt lgkmcnt(7)
	v_mfma_f32_32x32x16_bf16 v[66:81], v[204:207], v[102:105], 0
	ds_read_b128 v[204:207], v208 offset:12928
	s_waitcnt lgkmcnt(7)
	v_mfma_f32_32x32x16_bf16 v[82:97], v[210:213], v[98:101], v[82:97]
	ds_read_b128 v[210:213], v208 offset:4256
	s_waitcnt lgkmcnt(7)
	v_mfma_f32_32x32x16_bf16 v[66:81], v[214:217], v[98:101], v[66:81]
	ds_read_b128 v[214:217], v208 offset:12960
	s_waitcnt lgkmcnt(7)
	v_mfma_f32_32x32x16_bf16 v[82:97], v[218:221], v[110:113], v[82:97]
	ds_read_b128 v[218:221], v208 offset:4288
	s_waitcnt lgkmcnt(7)
	v_mfma_f32_32x32x16_bf16 v[66:81], v[222:225], v[110:113], v[66:81]
	ds_read_b128 v[222:225], v208 offset:12992
	s_waitcnt lgkmcnt(7)
	v_mfma_f32_32x32x16_bf16 v[82:97], v[226:229], v[106:109], v[82:97]
	ds_read_b128 v[226:229], v208 offset:4320
	s_waitcnt lgkmcnt(7)
	v_mfma_f32_32x32x16_bf16 v[66:81], v[230:233], v[106:109], v[66:81]
	ds_read_b128 v[230:233], v208 offset:13024
	s_waitcnt lgkmcnt(7)
	v_mfma_f32_32x32x16_bf16 v[82:97], v[200:203], v[118:121], v[82:97]
	s_waitcnt lgkmcnt(6)
	v_mfma_f32_32x32x16_bf16 v[66:81], v[204:207], v[118:121], v[66:81]
	s_waitcnt lgkmcnt(5)
	v_mfma_f32_32x32x16_bf16 v[82:97], v[210:213], v[114:117], v[82:97]
	s_waitcnt lgkmcnt(4)
	v_mfma_f32_32x32x16_bf16 v[66:81], v[214:217], v[114:117], v[66:81]
	s_waitcnt lgkmcnt(3)
	v_mfma_f32_32x32x16_bf16 v[82:97], v[218:221], v[126:129], v[82:97]
	s_waitcnt lgkmcnt(2)
	v_mfma_f32_32x32x16_bf16 v[66:81], v[222:225], v[126:129], v[66:81]
	v_cndmask_b32_e64 v196, 0, 1, s[6:7]
	v_cmp_ne_u32_e64 s[4:5], 1, v196
	s_waitcnt lgkmcnt(1)
	v_mfma_f32_32x32x16_bf16 v[82:97], v[226:229], v[122:125], v[82:97]
	s_waitcnt lgkmcnt(0)
	v_mfma_f32_32x32x16_bf16 v[66:81], v[230:233], v[122:125], v[66:81]
	s_cbranch_vccnz .LBB0_1785
	v_cmp_lt_i32_e32 vcc, v175, v194
	s_nop 7
	v_cndmask_b32_e32 v83, v169, v83, vcc
	v_cmp_le_i32_e32 vcc, v175, v194
	s_nop 1
	v_cndmask_b32_e32 v82, v169, v82, vcc
	v_cmp_le_i32_e32 vcc, v180, v194
	s_nop 1
	v_cndmask_b32_e32 v84, v169, v84, vcc
	v_cmp_le_i32_e32 vcc, v181, v194
	s_nop 1
	v_cndmask_b32_e32 v85, v169, v85, vcc
	v_cmp_le_i32_e32 vcc, v182, v194
	s_nop 1
	v_cndmask_b32_e32 v86, v169, v86, vcc
	v_cmp_le_i32_e32 vcc, v183, v194
	s_nop 1
	v_cndmask_b32_e32 v87, v169, v87, vcc
	v_cmp_le_i32_e32 vcc, v184, v194
	s_nop 1
	v_cndmask_b32_e32 v88, v169, v88, vcc
	v_cmp_le_i32_e32 vcc, v185, v194
	s_nop 1
	v_cndmask_b32_e32 v89, v169, v89, vcc
	v_cmp_le_i32_e32 vcc, v186, v194
	s_nop 1
	v_cndmask_b32_e32 v90, v169, v90, vcc
	v_cmp_le_i32_e32 vcc, v187, v194
	s_nop 1
	v_cndmask_b32_e32 v91, v169, v91, vcc
	v_cmp_le_i32_e32 vcc, v188, v194
	s_nop 1
	v_cndmask_b32_e32 v92, v169, v92, vcc
	v_cmp_le_i32_e32 vcc, v189, v194
	s_nop 1
	v_cndmask_b32_e32 v93, v169, v93, vcc
	v_cmp_le_i32_e32 vcc, v190, v194
	s_nop 1
	v_cndmask_b32_e32 v94, v169, v94, vcc
	v_cmp_le_i32_e32 vcc, v191, v194
	s_nop 1
	v_cndmask_b32_e32 v95, v169, v95, vcc
	v_cmp_le_i32_e32 vcc, v192, v194
	s_nop 1
	v_cndmask_b32_e32 v96, v169, v96, vcc
	v_cmp_le_i32_e32 vcc, v193, v194
	s_nop 1
	v_cndmask_b32_e32 v97, v169, v97, vcc
